# v5 + group barrier: L1 invalidate issued right after the arrival atomic (overlaps the wait for the other workgroups) instead of after the release is observed
# speedup vs baseline: 1.0028x; 1.0028x over previous
.LBB0_126:
	s_or_b64 exec, exec, s[38:39]
	buffer_inv sc1
	v_readlane_b32 s4, v254, 51
	v_readlane_b32 s5, v254, 52
	s_nop 4
	global_load_dword v1, v115, s[4:5] offset:2048 sc1
	s_lshl_b32 s4, s7, 3
	s_waitcnt vmcnt(0)
	v_cmp_le_u32_e32 vcc, s4, v1
	s_cbranch_vccnz .LBB0_139
	s_mov_b32 s5, 1
	s_branch .LBB0_129

.LBB0_139:
	s_waitcnt vmcnt(0)
	s_waitcnt vmcnt(0)

.LBB0_277:
	s_or_b64 exec, exec, s[28:29]
	buffer_inv sc1
	v_readlane_b32 s4, v254, 51
	v_readlane_b32 s5, v254, 52
	s_nop 4
	global_load_dword v1, v115, s[4:5] offset:2048 sc1
	s_lshl_b32 s4, s7, 3
	s_waitcnt vmcnt(0)
	v_cmp_le_u32_e32 vcc, s4, v1
	s_cbranch_vccnz .LBB0_290
	s_mov_b32 s5, 1
	s_branch .LBB0_280

.LBB0_1163:
	s_or_b64 exec, exec, s[10:11]
	buffer_inv sc1
	v_readlane_b32 s8, v254, 51
	v_readlane_b32 s9, v254, 52
	v_readlane_b32 s7, v255, 10
	s_lshl_b32 s7, s7, 3
	s_nop 2
	global_load_dword v1, v115, s[8:9] offset:2048 sc1
	s_waitcnt vmcnt(0)
	v_cmp_le_u32_e32 vcc, s7, v1
	s_cbranch_vccnz .LBB0_1176
	s_mov_b32 s12, 1
	s_branch .LBB0_1166

.LBB0_1298:
	s_or_b64 exec, exec, s[8:9]
	buffer_inv sc1
	v_readlane_b32 s4, v254, 51
	v_readlane_b32 s5, v254, 52
	s_nop 4
	global_load_dword v1, v115, s[4:5] offset:2048 sc1
	v_readlane_b32 s4, v255, 10
	s_lshl_b32 s7, s4, 3
	s_waitcnt vmcnt(0)
	v_cmp_le_u32_e32 vcc, s7, v1
	s_cbranch_vccnz .LBB0_1311
	s_mov_b32 s12, 1
	s_branch .LBB0_1301
